# speedup vs baseline: 1.0096x; 1.0096x over previous
.LBB0_14:
	s_waitcnt vmcnt(0)
	v_cvt_pk_bf16_f32 v21, v54, v58
	v_cvt_pk_bf16_f32 v20, v38, v42
	v_cvt_pk_bf16_f32 v19, v14, v22
	v_cvt_pk_bf16_f32 v18, v6, v10
	v_cvt_pk_bf16_f32 v33, v55, v59
	v_cvt_pk_bf16_f32 v32, v39, v43
	v_cvt_pk_bf16_f32 v31, v15, v23
	v_cvt_pk_bf16_f32 v30, v7, v11
	v_cvt_pk_bf16_f32 v49, v56, v60
	v_cvt_pk_bf16_f32 v48, v40, v44
	v_cvt_pk_bf16_f32 v47, v16, v24
	v_cvt_pk_bf16_f32 v46, v8, v12
	v_cvt_pk_bf16_f32 v43, v57, v61
	v_cvt_pk_bf16_f32 v42, v41, v45
	v_cvt_pk_bf16_f32 v41, v17, v25
	v_cvt_pk_bf16_f32 v40, v9, v13
	s_waitcnt lgkmcnt(1)
	v_mfma_f32_16x16x32_bf16 v[50:53], v[74:77], v[18:21], v[102:105]
	s_waitcnt lgkmcnt(0)
	v_mfma_f32_16x16x32_bf16 v[18:21], v[82:85], v[18:21], v[110:113]
	v_mfma_f32_16x16x32_bf16 v[62:65], v[74:77], v[30:33], v[94:97]
	v_mfma_f32_16x16x32_bf16 v[30:33], v[82:85], v[30:33], v[106:109]
	v_mfma_f32_16x16x32_bf16 v[66:69], v[74:77], v[46:49], v[90:93]
	v_mfma_f32_16x16x32_bf16 v[46:49], v[82:85], v[46:49], v[98:101]
	v_mfma_f32_16x16x32_bf16 v[10:13], v[74:77], v[40:43], v[70:73]
	v_mfma_f32_16x16x32_bf16 v[6:9], v[82:85], v[40:43], v[86:89]
	s_and_saveexec_b64 s[0:1], s[4:5]
	s_cbranch_execz .LBB0_16
	s_lshr_b32 s2, s2, 4
	v_lshrrev_b32_e32 v22, 1, v128
	v_mad_u64_u32 v[22:23], s[4:5], s2, 48, v[22:23]
	v_ashrrev_i32_e32 v23, 31, v22
	v_lshlrev_b64 v[22:23], 10, v[22:23]
	v_lshlrev_b32_e32 v24, 9, v126
	v_cvt_pk_bf16_f32 v16, v26, v27
	v_and_b32_e32 v26, 31, v132
	v_lshl_add_u64 v[22:23], s[16:17], 0, v[22:23]
	v_and_b32_e32 v24, 0x200, v24
	v_mov_b32_e32 v25, 0
	v_lshl_add_u64 v[22:23], v[22:23], 0, v[24:25]
	v_lshlrev_b32_e32 v24, 4, v26
	v_cvt_pk_bf16_f32 v17, v28, v29
	v_cvt_pk_bf16_f32 v15, v36, v37
	v_cvt_pk_bf16_f32 v14, v34, v35
	v_lshl_add_u64 v[22:23], v[22:23], 0, v[24:25]
	global_store_dwordx4 v[22:23], v[14:17], off sc0 sc1

.LBB0_18:
	s_or_b64 exec, exec, s[0:1]
	s_and_b32 s0, s3, 0x3ffffffc
	v_and_b32_e32 v1, 31, v0
	v_and_b32_e32 v2, 0x3e0, v0
	s_movk_i32 s2, 0x310
	s_or_b32 s0, s0, s22
	v_mad_u32_u24 v26, v1, s2, v2
	s_waitcnt lgkmcnt(0)
	s_barrier
	s_lshl_b32 s0, s0, 2
	ds_read_b128 v[2:5], v26
	ds_read_b128 v[6:9], v26 offset:16
	ds_read_b128 v[10:13], v26 offset:25088
	ds_read_b128 v[14:17], v26 offset:25104
	ds_read_b128 v[18:21], v26 offset:50176
	ds_read_b128 v[22:25], v26 offset:50192
	v_add_u32_e32 v27, 0x12600, v26
	v_add_u32_e32 v30, 0x12610, v26
	s_or_b32 s0, s0, s24
	ds_read_b128 v[26:29], v27
	ds_read_b128 v[30:33], v30
	s_mul_hi_i32 s1, s0, 0x3000
	s_mulk_i32 s0, 0x3000
	s_add_u32 s0, s8, s0
	s_waitcnt lgkmcnt(6)
	v_pk_add_f32 v[8:9], v[8:9], 0 op_sel_hi:[1,0]
	v_pk_add_f32 v[4:5], v[4:5], 0 op_sel_hi:[1,0]
	v_pk_add_f32 v[6:7], v[6:7], 0 op_sel_hi:[1,0]
	v_pk_add_f32 v[2:3], v[2:3], 0 op_sel_hi:[1,0]
	s_addc_u32 s1, s9, s1
	s_waitcnt lgkmcnt(5)
	v_pk_add_f32 v[4:5], v[4:5], v[12:13]
	s_waitcnt lgkmcnt(4)
	v_pk_add_f32 v[8:9], v[8:9], v[16:17]
	v_pk_add_f32 v[2:3], v[2:3], v[10:11]
	v_pk_add_f32 v[6:7], v[6:7], v[14:15]
	v_mov_b32_e32 v1, 0
	s_waitcnt lgkmcnt(2)
	v_pk_add_f32 v[8:9], v[8:9], v[24:25]
	v_pk_add_f32 v[4:5], v[4:5], v[20:21]
	v_pk_add_f32 v[6:7], v[6:7], v[22:23]
	v_pk_add_f32 v[2:3], v[2:3], v[18:19]
	s_cmp_eq_u32 s24, 0
	s_waitcnt lgkmcnt(1)
	v_pk_add_f32 v[10:11], v[4:5], v[28:29]
	s_waitcnt lgkmcnt(0)
	v_pk_add_f32 v[4:5], v[8:9], v[32:33]
	v_pk_add_f32 v[8:9], v[2:3], v[26:27]
	v_pk_add_f32 v[6:7], v[6:7], v[30:31]
	v_lshl_add_u64 v[12:13], v[0:1], 4, s[0:1]
	s_cselect_b64 s[0:1], -1, 0
	v_cmp_gt_u32_e32 vcc, 32, v0
	v_cvt_pk_bf16_f32 v5, v4, v5
	v_cvt_pk_bf16_f32 v3, v10, v11
	v_cvt_pk_bf16_f32 v4, v6, v7
	v_cvt_pk_bf16_f32 v2, v8, v9
	s_and_b64 s[0:1], s[0:1], vcc
	global_store_dwordx4 v[12:13], v[2:5], off sc0 sc1
	s_and_saveexec_b64 s[4:5], s[0:1]
	s_cbranch_execz .LBB0_20
	v_mov_b32_e32 v1, 0x18800
	v_lshl_add_u32 v1, v0, 2, v1
	ds_read2_b32 v[2:3], v1 offset1:32
	ds_read2_b32 v[4:5], v1 offset0:64 offset1:96
	v_lshl_or_b32 v0, s3, 5, v0
	v_ashrrev_i32_e32 v1, 31, v0
	v_lshl_add_u64 v[0:1], v[0:1], 2, s[10:11]
	s_waitcnt lgkmcnt(1)
	v_add_f32_e32 v2, 0, v2
	v_add_f32_e32 v2, v2, v3
	s_waitcnt lgkmcnt(0)
	v_add_f32_e32 v2, v2, v4
	v_add_f32_e32 v2, v2, v5
	global_store_dword v[0:1], v2, off sc0 sc1
